# helper LDS-read batching + low-rank prefetch + top-k scalar popcounts, with extra MFMA-to-VALU padding on the low-rank last-iteration path
# speedup vs baseline: 1.0015x; 1.0015x over previous
.Llr_nopref:
	s_nop 3
	v_add_u32_e32 v68, s12, v149
	v_ashrrev_i32_e32 v69, 31, v68
	v_lshlrev_b64 v[70:71], 2, v[68:69]
	v_lshl_add_u64 v[68:69], s[30:31], 0, v[70:71]
	v_lshl_add_u64 v[70:71], s[66:67], 0, v[70:71]
	global_load_dword v68, v[68:69], off
	s_nop 0
	global_load_dword v69, v[70:71], off
	v_add_f32_e32 v4, v147, v4
	v_mul_f32_e32 v4, 0xbfb8aa3b, v4
	v_exp_f32_e32 v4, v4
	v_add_u32_e32 v70, s0, v145
	v_subrev_u32_e32 v150, 32, v70
	v_add_f32_e32 v20, v148, v20
	v_add_f32_e32 v4, 1.0, v4
	v_rcp_f32_e32 v4, v4
	v_mov_b32_e32 v151, v3
	v_mul_f32_e32 v20, 0xbfb8aa3b, v20
	v_lshl_add_u64 v[152:153], v[150:151], 2, s[58:59]
	v_cvt_pk_bf16_f32 v4, v4, s0
	v_lshl_add_u64 v[150:151], v[150:151], 1, s[56:57]
	v_exp_f32_e32 v20, v20
	global_store_short v[150:151], v4, off
	v_add_f32_e32 v4, v148, v21
	v_mul_f32_e32 v4, 0xbfb8aa3b, v4
	v_exp_f32_e32 v4, v4
	v_add_f32_e32 v20, 1.0, v20
	v_rcp_f32_e32 v20, v20
	v_mov_b32_e32 v21, v3
	v_add_f32_e32 v4, 1.0, v4
	v_rcp_f32_e32 v4, v4
	v_mul_f32_e32 v20, 0xbf1b459e, v20
	v_mul_f32_e32 v20, 0x3fb8aa3b, v20
	v_exp_f32_e32 v20, v20
	v_mul_f32_e32 v4, 0xbf1b459e, v4
	v_mul_f32_e32 v4, 0x3fb8aa3b, v4
	v_exp_f32_e32 v4, v4
	global_store_dword v[152:153], v20, off
	v_add_u32_e32 v20, 0x3e0, v70
	v_lshl_add_u64 v[150:151], v[20:21], 2, s[58:59]
	global_store_dword v[150:151], v4, off
	v_add_f32_e32 v4, v147, v5
	v_mul_f32_e32 v4, 0xbfb8aa3b, v4
	v_exp_f32_e32 v4, v4
	v_add_f32_e32 v6, v147, v6
	v_mul_f32_e32 v6, 0xbfb8aa3b, v6
	v_exp_f32_e32 v6, v6
	v_add_f32_e32 v4, 1.0, v4
	v_rcp_f32_e32 v4, v4
	v_add_u32_e32 v2, 0xc00, v2
	v_add_f32_e32 v6, 1.0, v6
	v_rcp_f32_e32 v6, v6
	v_cvt_pk_bf16_f32 v71, v4, s0
	v_lshl_add_u64 v[4:5], v[20:21], 1, s[56:57]
	global_store_short v[4:5], v71, off
	v_add_f32_e32 v5, v148, v22
	v_mul_f32_e32 v5, 0xbfb8aa3b, v5
	v_exp_f32_e32 v5, v5
	v_add_u32_e32 v4, 0x7e0, v70
	v_cvt_pk_bf16_f32 v6, v6, s0
	v_add_f32_e32 v5, 1.0, v5
	v_rcp_f32_e32 v5, v5
	s_nop 0
	v_mul_f32_e32 v5, 0xbf1b459e, v5
	v_mul_f32_e32 v5, 0x3fb8aa3b, v5
	v_exp_f32_e32 v22, v5
	v_mov_b32_e32 v5, v3
	v_lshl_add_u64 v[20:21], v[4:5], 2, s[58:59]
	v_lshl_add_u64 v[4:5], v[4:5], 1, s[56:57]
	global_store_short v[4:5], v6, off
	v_add_f32_e32 v5, v148, v23
	v_mul_f32_e32 v5, 0xbfb8aa3b, v5
	v_exp_f32_e32 v5, v5
	v_add_u32_e32 v4, 0xbe0, v70
	global_store_dword v[20:21], v22, off
	v_add_f32_e32 v5, 1.0, v5
	v_rcp_f32_e32 v5, v5
	s_nop 0
	v_mul_f32_e32 v5, 0xbf1b459e, v5
	v_mul_f32_e32 v5, 0x3fb8aa3b, v5
	v_exp_f32_e32 v6, v5
	v_mov_b32_e32 v5, v3
	v_lshl_add_u64 v[20:21], v[4:5], 2, s[58:59]
	v_lshl_add_u64 v[4:5], v[4:5], 1, s[56:57]
	global_store_dword v[20:21], v6, off
	v_add_f32_e32 v6, v147, v7
	v_mul_f32_e32 v6, 0xbfb8aa3b, v6
	v_exp_f32_e32 v6, v6
	s_nop 0
	v_add_f32_e32 v6, 1.0, v6
	v_rcp_f32_e32 v6, v6
	s_nop 0
	v_cvt_pk_bf16_f32 v6, v6, s0
	global_store_short v[4:5], v6, off
	v_add_f32_e32 v5, v148, v24
	v_mul_f32_e32 v5, 0xbfb8aa3b, v5
	v_exp_f32_e32 v5, v5
	v_add_u32_e32 v4, 0x1fe0, v70
	v_add_f32_e32 v5, 1.0, v5
	v_rcp_f32_e32 v5, v5
	s_nop 0
	v_mul_f32_e32 v5, 0xbf1b459e, v5
	v_mul_f32_e32 v5, 0x3fb8aa3b, v5
	v_exp_f32_e32 v20, v5
	v_mov_b32_e32 v5, v3
	v_lshl_add_u64 v[6:7], v[4:5], 2, s[58:59]
	v_lshl_add_u64 v[4:5], v[4:5], 1, s[56:57]
	global_store_dword v[6:7], v20, off
	v_add_f32_e32 v6, v147, v8
	v_mul_f32_e32 v6, 0xbfb8aa3b, v6
	v_exp_f32_e32 v6, v6
	s_nop 0
	v_add_f32_e32 v6, 1.0, v6
	v_rcp_f32_e32 v6, v6
	s_nop 0
	v_cvt_pk_bf16_f32 v6, v6, s0
	global_store_short v[4:5], v6, off
	v_add_f32_e32 v5, v148, v25
	v_mul_f32_e32 v5, 0xbfb8aa3b, v5
	v_exp_f32_e32 v5, v5
	v_add_u32_e32 v4, 0x23e0, v70
	v_add_f32_e32 v5, 1.0, v5
	v_rcp_f32_e32 v5, v5
	s_nop 0
	v_mul_f32_e32 v5, 0xbf1b459e, v5
	v_mul_f32_e32 v5, 0x3fb8aa3b, v5
	v_exp_f32_e32 v8, v5
	v_mov_b32_e32 v5, v3
	v_lshl_add_u64 v[6:7], v[4:5], 2, s[58:59]
	v_lshl_add_u64 v[4:5], v[4:5], 1, s[56:57]
	global_store_dword v[6:7], v8, off
	v_add_f32_e32 v6, v147, v9
	v_mul_f32_e32 v6, 0xbfb8aa3b, v6
	v_exp_f32_e32 v6, v6
	s_nop 0
	v_add_f32_e32 v6, 1.0, v6
	v_rcp_f32_e32 v6, v6
	s_nop 0
	v_cvt_pk_bf16_f32 v6, v6, s0
	global_store_short v[4:5], v6, off
	v_add_f32_e32 v5, v148, v26
	v_mul_f32_e32 v5, 0xbfb8aa3b, v5
	v_exp_f32_e32 v5, v5
	v_add_u32_e32 v4, 0x27e0, v70
	v_add_f32_e32 v5, 1.0, v5
	v_rcp_f32_e32 v5, v5
	s_nop 0
	v_mul_f32_e32 v5, 0xbf1b459e, v5
	v_mul_f32_e32 v5, 0x3fb8aa3b, v5
	v_exp_f32_e32 v8, v5
	v_mov_b32_e32 v5, v3
	v_lshl_add_u64 v[6:7], v[4:5], 2, s[58:59]
	v_lshl_add_u64 v[4:5], v[4:5], 1, s[56:57]
	global_store_dword v[6:7], v8, off
	v_add_f32_e32 v6, v147, v10
	v_mul_f32_e32 v6, 0xbfb8aa3b, v6
	v_exp_f32_e32 v6, v6
	s_nop 0
	v_add_f32_e32 v6, 1.0, v6
	v_rcp_f32_e32 v6, v6
	s_nop 0
	v_cvt_pk_bf16_f32 v6, v6, s0
	global_store_short v[4:5], v6, off
	v_add_f32_e32 v5, v148, v27
	v_mul_f32_e32 v5, 0xbfb8aa3b, v5
	v_exp_f32_e32 v5, v5
	v_add_u32_e32 v4, 0x2be0, v70
	v_add_f32_e32 v5, 1.0, v5
	v_rcp_f32_e32 v5, v5
	s_nop 0
	v_mul_f32_e32 v5, 0xbf1b459e, v5
	v_mul_f32_e32 v5, 0x3fb8aa3b, v5
	v_exp_f32_e32 v8, v5
	v_mov_b32_e32 v5, v3
	v_lshl_add_u64 v[6:7], v[4:5], 2, s[58:59]
	v_lshl_add_u64 v[4:5], v[4:5], 1, s[56:57]
	global_store_dword v[6:7], v8, off
	v_add_f32_e32 v6, v147, v11
	v_mul_f32_e32 v6, 0xbfb8aa3b, v6
	v_exp_f32_e32 v6, v6
	s_nop 0
	v_add_f32_e32 v6, 1.0, v6
	v_rcp_f32_e32 v6, v6
	s_nop 0
	v_cvt_pk_bf16_f32 v6, v6, s0
	global_store_short v[4:5], v6, off
	v_add_f32_e32 v5, v148, v28
	v_mul_f32_e32 v5, 0xbfb8aa3b, v5
	v_exp_f32_e32 v5, v5
	v_add_u32_e32 v4, 0x3fe0, v70
	v_add_f32_e32 v5, 1.0, v5
	v_rcp_f32_e32 v5, v5
	s_nop 0
	v_mul_f32_e32 v5, 0xbf1b459e, v5
	v_mul_f32_e32 v5, 0x3fb8aa3b, v5
	v_exp_f32_e32 v8, v5
	v_mov_b32_e32 v5, v3
	v_lshl_add_u64 v[6:7], v[4:5], 2, s[58:59]
	v_lshl_add_u64 v[4:5], v[4:5], 1, s[56:57]
	global_store_dword v[6:7], v8, off
	v_add_f32_e32 v6, v147, v12
	v_mul_f32_e32 v6, 0xbfb8aa3b, v6
	v_exp_f32_e32 v6, v6
	s_nop 0
	v_add_f32_e32 v6, 1.0, v6
	v_rcp_f32_e32 v6, v6
	s_nop 0
	v_cvt_pk_bf16_f32 v6, v6, s0
	global_store_short v[4:5], v6, off
	v_add_f32_e32 v5, v148, v29
	v_mul_f32_e32 v5, 0xbfb8aa3b, v5
	v_exp_f32_e32 v5, v5
	v_add_u32_e32 v4, 0x43e0, v70
	v_add_f32_e32 v5, 1.0, v5
	v_rcp_f32_e32 v5, v5
	s_nop 0
	v_mul_f32_e32 v5, 0xbf1b459e, v5
	v_mul_f32_e32 v5, 0x3fb8aa3b, v5
	v_exp_f32_e32 v8, v5
	v_mov_b32_e32 v5, v3
	v_lshl_add_u64 v[6:7], v[4:5], 2, s[58:59]
	v_lshl_add_u64 v[4:5], v[4:5], 1, s[56:57]
	global_store_dword v[6:7], v8, off
	v_add_f32_e32 v6, v147, v13
	v_mul_f32_e32 v6, 0xbfb8aa3b, v6
	v_exp_f32_e32 v6, v6
	s_nop 0
	v_add_f32_e32 v6, 1.0, v6
	v_rcp_f32_e32 v6, v6
	s_nop 0
	v_cvt_pk_bf16_f32 v6, v6, s0
	global_store_short v[4:5], v6, off
	v_add_f32_e32 v5, v148, v30
	v_mul_f32_e32 v5, 0xbfb8aa3b, v5
	v_exp_f32_e32 v5, v5
	v_add_u32_e32 v4, 0x47e0, v70
	v_add_f32_e32 v5, 1.0, v5
	v_rcp_f32_e32 v5, v5
	s_nop 0
	v_mul_f32_e32 v5, 0xbf1b459e, v5
	v_mul_f32_e32 v5, 0x3fb8aa3b, v5
	v_exp_f32_e32 v8, v5
	v_mov_b32_e32 v5, v3
	v_lshl_add_u64 v[6:7], v[4:5], 2, s[58:59]
	v_lshl_add_u64 v[4:5], v[4:5], 1, s[56:57]
	global_store_dword v[6:7], v8, off
	v_add_f32_e32 v6, v147, v14
	v_mul_f32_e32 v6, 0xbfb8aa3b, v6
	v_exp_f32_e32 v6, v6
	s_nop 0
	v_add_f32_e32 v6, 1.0, v6
	v_rcp_f32_e32 v6, v6
	s_nop 0
	v_cvt_pk_bf16_f32 v6, v6, s0
	global_store_short v[4:5], v6, off
	v_add_f32_e32 v5, v148, v31
	v_mul_f32_e32 v5, 0xbfb8aa3b, v5
	v_exp_f32_e32 v5, v5
	v_add_u32_e32 v4, 0x4be0, v70
	v_add_f32_e32 v5, 1.0, v5
	v_rcp_f32_e32 v5, v5
	s_nop 0
	v_mul_f32_e32 v5, 0xbf1b459e, v5
	v_mul_f32_e32 v5, 0x3fb8aa3b, v5
	v_exp_f32_e32 v8, v5
	v_mov_b32_e32 v5, v3
	v_lshl_add_u64 v[6:7], v[4:5], 2, s[58:59]
	v_lshl_add_u64 v[4:5], v[4:5], 1, s[56:57]
	global_store_dword v[6:7], v8, off
	v_add_f32_e32 v6, v147, v15
	v_mul_f32_e32 v6, 0xbfb8aa3b, v6
	v_exp_f32_e32 v6, v6
	s_nop 0
	v_add_f32_e32 v6, 1.0, v6
	v_rcp_f32_e32 v6, v6
	s_nop 0
	v_cvt_pk_bf16_f32 v6, v6, s0
	global_store_short v[4:5], v6, off
	v_add_f32_e32 v5, v148, v32
	v_mul_f32_e32 v5, 0xbfb8aa3b, v5
	v_exp_f32_e32 v5, v5
	v_add_u32_e32 v4, 0x5fe0, v70
	v_add_f32_e32 v5, 1.0, v5
	v_rcp_f32_e32 v5, v5
	s_nop 0
	v_mul_f32_e32 v5, 0xbf1b459e, v5
	v_mul_f32_e32 v5, 0x3fb8aa3b, v5
	v_exp_f32_e32 v8, v5
	v_mov_b32_e32 v5, v3
	v_lshl_add_u64 v[6:7], v[4:5], 2, s[58:59]
	v_lshl_add_u64 v[4:5], v[4:5], 1, s[56:57]
	global_store_dword v[6:7], v8, off
	v_add_f32_e32 v6, v147, v16
	v_mul_f32_e32 v6, 0xbfb8aa3b, v6
	v_exp_f32_e32 v6, v6
	s_nop 0
	v_add_f32_e32 v6, 1.0, v6
	v_rcp_f32_e32 v6, v6
	s_nop 0
	v_cvt_pk_bf16_f32 v6, v6, s0
	global_store_short v[4:5], v6, off
	v_add_f32_e32 v5, v148, v33
	v_mul_f32_e32 v5, 0xbfb8aa3b, v5
	v_exp_f32_e32 v5, v5
	v_add_u32_e32 v4, 0x63e0, v70
	v_add_f32_e32 v5, 1.0, v5
	v_rcp_f32_e32 v5, v5
	s_nop 0
	v_mul_f32_e32 v5, 0xbf1b459e, v5
	v_mul_f32_e32 v5, 0x3fb8aa3b, v5
	v_exp_f32_e32 v8, v5
	v_mov_b32_e32 v5, v3
	v_lshl_add_u64 v[6:7], v[4:5], 2, s[58:59]
	v_lshl_add_u64 v[4:5], v[4:5], 1, s[56:57]
	global_store_dword v[6:7], v8, off
	v_add_f32_e32 v6, v147, v17
	v_mul_f32_e32 v6, 0xbfb8aa3b, v6
	v_exp_f32_e32 v6, v6
	s_nop 0
	v_add_f32_e32 v6, 1.0, v6
	v_rcp_f32_e32 v6, v6
	s_nop 0
	v_cvt_pk_bf16_f32 v6, v6, s0
	global_store_short v[4:5], v6, off
	v_add_f32_e32 v5, v148, v34
	v_mul_f32_e32 v5, 0xbfb8aa3b, v5
	v_exp_f32_e32 v5, v5
	v_add_u32_e32 v4, 0x67e0, v70
	v_add_f32_e32 v5, 1.0, v5
	v_rcp_f32_e32 v5, v5
	s_nop 0
	v_mul_f32_e32 v5, 0xbf1b459e, v5
	v_mul_f32_e32 v5, 0x3fb8aa3b, v5
	v_exp_f32_e32 v8, v5
	v_mov_b32_e32 v5, v3
	v_lshl_add_u64 v[6:7], v[4:5], 2, s[58:59]
	v_lshl_add_u64 v[4:5], v[4:5], 1, s[56:57]
	global_store_dword v[6:7], v8, off
	v_add_f32_e32 v6, v147, v18
	v_mul_f32_e32 v6, 0xbfb8aa3b, v6
	v_exp_f32_e32 v6, v6
	s_nop 0
	v_add_f32_e32 v6, 1.0, v6
	v_rcp_f32_e32 v6, v6
	s_nop 0
	v_cvt_pk_bf16_f32 v6, v6, s0
	global_store_short v[4:5], v6, off
	v_add_f32_e32 v5, v148, v35
	v_mul_f32_e32 v5, 0xbfb8aa3b, v5
	v_exp_f32_e32 v5, v5
	v_add_u32_e32 v4, 0x6be0, v70
	s_waitcnt vmcnt(31)
	v_mov_b32_e32 v148, v68
	v_add_f32_e32 v5, 1.0, v5
	v_rcp_f32_e32 v5, v5
	s_nop 0
	v_mul_f32_e32 v5, 0xbf1b459e, v5
	v_mul_f32_e32 v5, 0x3fb8aa3b, v5
	v_exp_f32_e32 v8, v5
	v_mov_b32_e32 v5, v3
	v_lshl_add_u64 v[6:7], v[4:5], 2, s[58:59]
	v_lshl_add_u64 v[4:5], v[4:5], 1, s[56:57]
	global_store_dword v[6:7], v8, off
	v_add_f32_e32 v6, v147, v19
	v_mul_f32_e32 v6, 0xbfb8aa3b, v6
	v_exp_f32_e32 v6, v6
	s_waitcnt vmcnt(31)
	v_mov_b32_e32 v147, v69
	v_add_f32_e32 v6, 1.0, v6
	v_rcp_f32_e32 v6, v6
	s_nop 0
	v_cvt_pk_bf16_f32 v6, v6, s0
	s_add_i32 s0, s0, 32
	s_cmpk_lg_i32 s0, 0xa0
	global_store_short v[4:5], v6, off
	s_cbranch_scc1 .LBB0_285
	s_add_i32 s14, s14, s97
	s_cmpk_gt_i32 s14, 0x1ff
	v_add_u32_e32 v145, s90, v145
	s_barrier
	s_cbranch_scc0 .LBB0_282
